# v15 + attention P fragments without cross-half exchange (V rows stored in natural key order)
# speedup vs baseline: 1.0132x; 1.0028x over previous
.LBB0_639:
	s_ashr_i32 s18, s33, 7
	s_lshl_b32 s68, s18, 12
	s_lshl_b32 s4, s33, 8
	s_and_b32 s4, s4, 0xf00
	s_add_i32 s5, s68, s22
	s_add_i32 s16, s5, s4
	s_bfe_u32 s19, s33, 0x30004
	s_ashr_i32 s17, s16, 31
	s_mul_i32 s5, s16, 0x3200
	s_mul_hi_i32 s4, s16, 0x3200
	s_add_u32 s5, s20, s5
	s_addc_u32 s4, s21, s4
	s_lshl_b32 s65, s19, 8
	s_add_u32 s5, s5, s65
	s_addc_u32 s65, s4, 0
	s_add_u32 s4, s5, 0x1800
	s_addc_u32 s5, s65, 0
	v_xor_b32_e32 v6, 0x80, v164
	v_mov_b32_e32 v7, 0
	v_xor_b32_e32 v8, 0x80, v168
	v_mov_b32_e32 v9, 0
	v_lshl_add_u64 v[2:3], s[4:5], 0, v[162:163]
	s_mov_b32 m0, s24
	v_lshl_add_u64 v[4:5], v[2:3], 0, v[164:165]
	s_lshl_b32 s66, s18, 8
	global_load_lds_dwordx4 v[4:5], off
	v_lshl_add_u64 v[4:5], s[4:5], 0, v[166:167]
	v_lshl_add_u64 v[4:5], v[4:5], 0, v[168:169]
	s_mov_b32 m0, s35
	s_addk_i32 s66, 0x4000
	global_load_lds_dwordx4 v[4:5], off
	v_lshl_add_u64 v[4:5], v[2:3], 0, s[6:7]
	v_lshl_add_u64 v[4:5], v[4:5], 0, v[6:7]
	s_mov_b32 m0, s36
	s_lshl_b32 s65, s19, 7
	global_load_lds_dwordx4 v[4:5], off
	v_lshl_add_u64 v[4:5], s[4:5], 0, v[170:171]
	v_lshl_add_u64 v[4:5], v[4:5], 0, v[8:9]
	s_mov_b32 m0, s37
	v_mov_b32_e32 v12, v177
	global_load_lds_dwordx4 v[4:5], off
	v_lshl_add_u64 v[4:5], v[2:3], 0, s[8:9]
	v_lshl_add_u64 v[4:5], v[4:5], 0, v[164:165]
	s_mov_b32 m0, s38
	s_mov_b32 s70, 0
	global_load_lds_dwordx4 v[4:5], off
	v_lshl_add_u64 v[4:5], s[4:5], 0, v[172:173]
	v_lshl_add_u64 v[4:5], v[4:5], 0, v[168:169]
	s_mov_b32 m0, s39
	s_nop 0
	global_load_lds_dwordx4 v[4:5], off
	v_lshl_add_u64 v[4:5], v[2:3], 0, s[10:11]
	v_lshl_add_u64 v[4:5], v[4:5], 0, v[6:7]
	s_mov_b32 m0, s40
	s_nop 0
	global_load_lds_dwordx4 v[4:5], off
	v_lshl_add_u64 v[4:5], s[4:5], 0, v[174:175]
	v_lshl_add_u64 v[4:5], v[4:5], 0, v[8:9]
	s_mov_b32 m0, s41
	s_mul_i32 s4, s66, 0x3200
	global_load_lds_dwordx4 v[4:5], off
	v_mov_b32_e32 v2, v196
	s_mul_hi_i32 s5, s66, 0x3200
	v_ashrrev_i32_e32 v3, 4, v2
	s_add_u32 s4, s20, s4
	v_and_b32_e32 v4, 15, v2
	v_add_u32_e32 v8, s25, v3
	s_addc_u32 s5, s21, s5
	s_or_b32 s67, s65, 0x1000
	v_bitop3_b32 v9, v8, v4, 15 bitop3:0x6c
	v_mul_lo_u32 v8, v8, s44
	v_ashrrev_i32_e32 v5, 5, v2
	v_add_u32_e32 v8, s67, v8
	v_lshlrev_b32_e32 v9, 4, v9
	v_bfe_u32 v6, v2, 2, 3
	v_lshrrev_b32_e32 v7, 1, v2
	v_lshl_or_b32 v8, v8, 1, v9
	v_add_u32_e32 v9, s26, v5
	v_lshlrev_b32_e32 v7, 3, v2
	v_lshlrev_b32_e32 v10, 1, v9
	v_and_b32_e32 v7, 24, v7
	v_and_b32_e32 v10, 0xfffff0, v10
	v_and_b32_e32 v9, 4, v9
	v_lshlrev_b32_e32 v9, 1, v9
	v_and_b32_e32 v2, 0x60, v2
	v_or3_b32 v9, v9, v10, v6
	v_or3_b32 v2, s65, v2, v7
	v_mad_u32_u24 v2, v9, s44, v2
	s_mov_b32 m0, s54
	v_lshl_add_u32 v2, v2, 1, v198
	global_load_lds_dwordx4 v8, s[4:5]
	s_mov_b32 m0, s53
	s_mov_b32 s71, 64
	global_load_lds_dwordx4 v2, s[4:5]
	v_add_u32_e32 v2, s28, v3
	v_mul_lo_u32 v3, v2, s44
	v_bitop3_b32 v2, v2, v4, 15 bitop3:0x6c
	v_add_u32_e32 v3, s67, v3
	v_lshlrev_b32_e32 v2, 4, v2
	v_lshl_or_b32 v2, v3, 1, v2
	v_add_u32_e32 v3, s29, v5
	v_lshlrev_b32_e32 v4, 1, v3
	v_and_b32_e32 v5, 4, v3
	v_lshlrev_b32_e32 v5, 1, v5
	v_lshlrev_b32_e32 v3, 5, v3
	v_and_b32_e32 v4, 0xfffff0, v4
	v_and_b32_e32 v3, 0x60, v3
	v_or3_b32 v4, v5, v4, v6
	v_or3_b32 v3, v7, v3, s65
	v_mad_u32_u24 v3, v4, s44, v3
	s_mov_b32 m0, s64
	v_lshl_add_u32 v3, v3, 1, v198
	global_load_lds_dwordx4 v2, s[4:5]
	s_mov_b32 m0, s55
	v_mov_b32_e32 v2, v176
	global_load_lds_dwordx4 v3, s[4:5]
	s_lshl_b32 s4, s18, 4
	s_lshl_b32 s5, s19, 1
	s_or_b32 s4, s5, s4
	s_ashr_i32 s5, s4, 31
	s_lshl_b64 s[4:5], s[4:5], 2
	s_add_u32 s18, s31, s4
	s_addc_u32 s19, s34, s5
	s_add_u32 s4, s88, s4
	s_addc_u32 s5, s89, s5
	global_load_dword v10, v163, s[18:19]
	global_load_dword v11, v199, s[4:5] offset:4
	s_waitcnt vmcnt(0)
	s_waitcnt vmcnt(0) lgkmcnt(0)
	s_barrier
	v_mov_b32_e32 v207, 0
	v_lshlrev_b32_e32 v3, 4, v2
	v_lshlrev_b32_e32 v13, 7, v12
	v_and_b32_e32 v14, 0xf0, v3
	v_lshl_add_u32 v15, v2, 8, s24
	v_xad_u32 v2, v13, v14, v15
	ds_read_b128 v[2:5], v2
	v_or_b32_e32 v6, 16, v13
	v_xad_u32 v6, v6, v14, v15
	ds_read_b128 v[6:9], v6
	v_cmp_eq_u32_e32 vcc, 0, v12
	s_waitcnt lgkmcnt(1)
	v_lshlrev_b32_e32 v16, 16, v2
	v_and_b32_e32 v2, 0xffff0000, v2
	v_mul_f32_e32 v2, v2, v2
	v_fmac_f32_e32 v2, v16, v16
	v_lshlrev_b32_e32 v16, 16, v3
	v_and_b32_e32 v3, 0xffff0000, v3
	v_mul_f32_e32 v3, v3, v3
	v_fmac_f32_e32 v3, v16, v16
	v_add_f32_e32 v2, v2, v3
	v_lshlrev_b32_e32 v3, 16, v4
	v_and_b32_e32 v4, 0xffff0000, v4
	v_mul_f32_e32 v4, v4, v4
	v_fmac_f32_e32 v4, v3, v3
	v_add_f32_e32 v2, v4, v2
	v_and_b32_e32 v4, 0xffff0000, v5
	v_lshlrev_b32_e32 v3, 16, v5
	v_mul_f32_e32 v4, v4, v4
	v_fmac_f32_e32 v4, v3, v3
	v_add_f32_e32 v2, v4, v2
	s_waitcnt lgkmcnt(0)
	v_and_b32_e32 v4, 0xffff0000, v6
	v_lshlrev_b32_e32 v3, 16, v6
	v_mul_f32_e32 v4, v4, v4
	v_fmac_f32_e32 v4, v3, v3
	v_add_f32_e32 v2, v4, v2
	v_and_b32_e32 v4, 0xffff0000, v7
	v_lshlrev_b32_e32 v3, 16, v7
	v_mul_f32_e32 v4, v4, v4
	v_fmac_f32_e32 v4, v3, v3
	v_add_f32_e32 v2, v4, v2
	v_and_b32_e32 v4, 0xffff0000, v8
	v_lshlrev_b32_e32 v3, 16, v8
	v_mul_f32_e32 v4, v4, v4
	v_fmac_f32_e32 v4, v3, v3
	v_and_b32_e32 v3, 0xffff0000, v9
	v_add_f32_e32 v6, v4, v2
	v_lshlrev_b32_e32 v2, 16, v9
	v_mul_f32_e32 v7, v3, v3
	v_fmac_f32_e32 v7, v2, v2
	v_or_b32_e32 v2, 32, v13
	v_xad_u32 v2, v2, v14, v15
	ds_read_b128 v[2:5], v2
	v_add_f32_e32 v16, v7, v6
	v_or_b32_e32 v6, 48, v13
	v_xad_u32 v6, v6, v14, v15
	ds_read_b128 v[6:9], v6
	s_waitcnt lgkmcnt(1)
	v_lshlrev_b32_e32 v17, 16, v2
	v_and_b32_e32 v2, 0xffff0000, v2
	v_mul_f32_e32 v2, v2, v2
	v_fmac_f32_e32 v2, v17, v17
	v_add_f32_e32 v2, v2, v16
	v_lshlrev_b32_e32 v16, 16, v3
	v_and_b32_e32 v3, 0xffff0000, v3
	v_mul_f32_e32 v3, v3, v3
	v_fmac_f32_e32 v3, v16, v16
	v_add_f32_e32 v2, v3, v2
	v_lshlrev_b32_e32 v3, 16, v4
	v_and_b32_e32 v4, 0xffff0000, v4
	v_mul_f32_e32 v4, v4, v4
	v_fmac_f32_e32 v4, v3, v3
	v_add_f32_e32 v2, v4, v2
	v_and_b32_e32 v4, 0xffff0000, v5
	v_lshlrev_b32_e32 v3, 16, v5
	v_mul_f32_e32 v4, v4, v4
	v_fmac_f32_e32 v4, v3, v3
	v_add_f32_e32 v2, v4, v2
	s_waitcnt lgkmcnt(0)
	v_and_b32_e32 v4, 0xffff0000, v6
	v_lshlrev_b32_e32 v3, 16, v6
	v_mul_f32_e32 v4, v4, v4
	v_fmac_f32_e32 v4, v3, v3
	v_add_f32_e32 v2, v4, v2
	v_and_b32_e32 v4, 0xffff0000, v7
	v_lshlrev_b32_e32 v3, 16, v7
	v_mul_f32_e32 v4, v4, v4
	v_fmac_f32_e32 v4, v3, v3
	v_add_f32_e32 v2, v4, v2
	v_and_b32_e32 v4, 0xffff0000, v8
	v_lshlrev_b32_e32 v3, 16, v8
	v_mul_f32_e32 v4, v4, v4
	v_fmac_f32_e32 v4, v3, v3
	v_and_b32_e32 v3, 0xffff0000, v9
	v_add_f32_e32 v6, v4, v2
	v_lshlrev_b32_e32 v2, 16, v9
	v_mul_f32_e32 v7, v3, v3
	v_fmac_f32_e32 v7, v2, v2
	v_or_b32_e32 v2, 64, v13
	v_xad_u32 v2, v2, v14, v15
	ds_read_b128 v[2:5], v2
	v_add_f32_e32 v16, v7, v6
	v_or_b32_e32 v6, 0x50, v13
	v_xad_u32 v6, v6, v14, v15
	ds_read_b128 v[6:9], v6
	s_waitcnt lgkmcnt(1)
	v_lshlrev_b32_e32 v17, 16, v2
	v_and_b32_e32 v2, 0xffff0000, v2
	v_mul_f32_e32 v2, v2, v2
	v_fmac_f32_e32 v2, v17, v17
	v_add_f32_e32 v2, v2, v16
	v_lshlrev_b32_e32 v16, 16, v3
	v_and_b32_e32 v3, 0xffff0000, v3
	v_mul_f32_e32 v3, v3, v3
	v_fmac_f32_e32 v3, v16, v16
	v_add_f32_e32 v2, v3, v2
	v_lshlrev_b32_e32 v3, 16, v4
	v_and_b32_e32 v4, 0xffff0000, v4
	v_mul_f32_e32 v4, v4, v4
	v_fmac_f32_e32 v4, v3, v3
	v_add_f32_e32 v2, v4, v2
	v_and_b32_e32 v4, 0xffff0000, v5
	v_lshlrev_b32_e32 v3, 16, v5
	v_mul_f32_e32 v4, v4, v4
	v_fmac_f32_e32 v4, v3, v3
	v_add_f32_e32 v2, v4, v2
	s_waitcnt lgkmcnt(0)
	v_and_b32_e32 v4, 0xffff0000, v6
	v_lshlrev_b32_e32 v3, 16, v6
	v_mul_f32_e32 v4, v4, v4
	v_fmac_f32_e32 v4, v3, v3
	v_add_f32_e32 v2, v4, v2
	v_and_b32_e32 v4, 0xffff0000, v7
	v_lshlrev_b32_e32 v3, 16, v7
	v_mul_f32_e32 v4, v4, v4
	v_fmac_f32_e32 v4, v3, v3
	v_add_f32_e32 v2, v4, v2
	v_and_b32_e32 v4, 0xffff0000, v8
	v_lshlrev_b32_e32 v3, 16, v8
	v_mul_f32_e32 v4, v4, v4
	v_fmac_f32_e32 v4, v3, v3
	v_and_b32_e32 v3, 0xffff0000, v9
	v_add_f32_e32 v6, v4, v2
	v_lshlrev_b32_e32 v2, 16, v9
	v_mul_f32_e32 v7, v3, v3
	v_fmac_f32_e32 v7, v2, v2
	v_or_b32_e32 v2, 0x60, v13
	v_xad_u32 v2, v2, v14, v15
	ds_read_b128 v[2:5], v2
	v_add_f32_e32 v16, v7, v6
	v_or_b32_e32 v6, 0x70, v13
	v_xad_u32 v6, v6, v14, v15
	ds_read_b128 v[6:9], v6
	s_waitcnt lgkmcnt(1)
	v_lshlrev_b32_e32 v13, 16, v2
	v_and_b32_e32 v2, 0xffff0000, v2
	v_mul_f32_e32 v2, v2, v2
	v_fmac_f32_e32 v2, v13, v13
	v_lshlrev_b32_e32 v13, 16, v3
	v_and_b32_e32 v3, 0xffff0000, v3
	v_mul_f32_e32 v3, v3, v3
	v_add_f32_e32 v2, v2, v16
	v_fmac_f32_e32 v3, v13, v13
	v_add_f32_e32 v2, v3, v2
	v_lshlrev_b32_e32 v3, 16, v4
	v_and_b32_e32 v4, 0xffff0000, v4
	v_mul_f32_e32 v4, v4, v4
	v_fmac_f32_e32 v4, v3, v3
	v_add_f32_e32 v2, v4, v2
	v_and_b32_e32 v4, 0xffff0000, v5
	v_lshlrev_b32_e32 v3, 16, v5
	v_mul_f32_e32 v4, v4, v4
	v_fmac_f32_e32 v4, v3, v3
	v_add_f32_e32 v13, v4, v2
	s_waitcnt lgkmcnt(0)
	v_and_b32_e32 v5, 0xffff0000, v7
	v_and_b32_e32 v4, 0xffff0000, v6
	v_lshlrev_b32_e32 v3, 16, v7
	v_lshlrev_b32_e32 v2, 16, v6
	v_pk_mul_f32 v[4:5], v[4:5], v[4:5]
	v_mov_b32_e32 v206, 0
	v_pk_fma_f32 v[2:3], v[2:3], v[2:3], v[4:5]
	v_and_b32_e32 v5, 0xffff0000, v9
	v_add_f32_e32 v2, v2, v13
	v_and_b32_e32 v4, 0xffff0000, v8
	v_add_f32_e32 v6, v3, v2
	v_lshlrev_b32_e32 v3, 16, v9
	v_lshlrev_b32_e32 v2, 16, v8
	v_pk_mul_f32 v[4:5], v[4:5], v[4:5]
	s_mov_b32 s72, 0
	v_pk_fma_f32 v[2:3], v[2:3], v[2:3], v[4:5]
	v_mov_b32_e32 v7, v163
	v_add_f32_e32 v2, v2, v6
	v_add_f32_e32 v2, v3, v2
	v_cndmask_b32_e32 v3, v11, v10, vcc
	v_mul_f32_e32 v2, v3, v2
	v_mul_f32_e32 v3, 0x4f800000, v2
	v_cmp_gt_f32_e32 vcc, s45, v2
	v_mov_b32_e32 v6, v163
	v_mov_b32_e32 v8, v163
	v_cndmask_b32_e32 v2, v2, v3, vcc
	v_sqrt_f32_e32 v3, v2
	v_mov_b32_e32 v9, v163
	v_mov_b32_e32 v10, v163
	v_mov_b32_e32 v11, v163
	v_add_u32_e32 v4, -1, v3
	v_fma_f32 v5, -v4, v3, v2
	v_cmp_ge_f32_e64 s[4:5], 0, v5
	v_add_u32_e32 v5, 1, v3
	v_mov_b32_e32 v12, v163
	v_cndmask_b32_e64 v4, v3, v4, s[4:5]
	v_fma_f32 v3, -v5, v3, v2
	v_cmp_lt_f32_e64 s[4:5], 0, v3
	v_mov_b32_e32 v13, v163
	v_mov_b32_e32 v14, v163
	v_cndmask_b32_e64 v3, v4, v5, s[4:5]
	v_mul_f32_e32 v4, 0x37800000, v3
	v_cndmask_b32_e32 v3, v3, v4, vcc
	v_cmp_class_f32_e32 vcc, v2, v200
	v_mov_b32_e32 v4, v163
	v_mov_b32_e32 v5, v163
	v_cndmask_b32_e32 v2, v3, v2, vcc
	v_mov_b32_e32 v3, v2
	s_nop 1
	v_permlane32_swap_b32_e32 v2, v3
	v_fmamk_f32 v2, v2, 0x3f8147ae, v201
	v_max_f32_e32 v204, 0, v2
	v_fmamk_f32 v2, v3, 0x3f8147ae, v201
	v_max_f32_e32 v205, 0, v2
	v_cmp_eq_f32_e32 vcc, 0, v204
	v_cmp_eq_f32_e64 s[4:5], 0, v205
	s_and_b64 s[4:5], vcc, s[4:5]
	v_mov_b32_e32 v3, v163
	v_cndmask_b32_e64 v2, 0, 1, s[4:5]
	v_cmp_ne_u32_e32 vcc, 0, v2
	s_cmp_eq_u64 vcc, exec
	s_cselect_b64 s[4:5], -1, 0
	v_cndmask_b32_e64 v2, 0, 1, s[4:5]
	v_mov_b32_e32 v15, v163
	v_readfirstlane_b32 s4, v2
	s_bitcmp1_b32 s4, 0
	s_cselect_b64 s[4:5], -1, 0
	s_xor_b64 s[4:5], s[4:5], -1
	v_cndmask_b32_e64 v208, 0, 1, s[4:5]
	s_addk_i32 s68, 0xff00
	s_or_b32 s69, s65, 0x1400
	v_mov_b32_e32 v2, 0
	v_mov_b32_e32 v16, v163
	v_mov_b32_e32 v17, v163
	v_mov_b32_e32 v18, 0
	v_mov_b32_e32 v19, v163
	v_mov_b32_e32 v20, v163
	v_mov_b32_e32 v21, v163
	v_mov_b32_e32 v22, v163
	v_mov_b32_e32 v23, v163
	v_mov_b32_e32 v24, v163
	v_mov_b32_e32 v25, v163
	v_mov_b32_e32 v26, v163
	v_mov_b32_e32 v27, v163
	v_mov_b32_e32 v28, v163
	v_mov_b32_e32 v29, v163
	v_mov_b32_e32 v30, v163
	v_mov_b32_e32 v31, v163
	v_mov_b32_e32 v32, v163
	v_mov_b32_e32 v33, v163
	v_mov_b32_e32 v34, 0
	v_mov_b32_e32 v35, v163
	v_mov_b32_e32 v36, v163
	v_mov_b32_e32 v37, v163
	v_mov_b32_e32 v38, v163
	v_mov_b32_e32 v39, v163
	v_mov_b32_e32 v40, v163
	v_mov_b32_e32 v41, v163
	v_mov_b32_e32 v42, v163
	v_mov_b32_e32 v43, v163
	v_mov_b32_e32 v44, v163
	v_mov_b32_e32 v45, v163
	v_mov_b32_e32 v46, v163
	v_mov_b32_e32 v47, v163
	v_mov_b32_e32 v48, v163
	v_mov_b32_e32 v49, v163
	v_mov_b32_e32 v50, 0
	v_mov_b32_e32 v51, v163
	v_mov_b32_e32 v52, v163
	v_mov_b32_e32 v53, v163
	v_mov_b32_e32 v54, v163
	v_mov_b32_e32 v55, v163
	v_mov_b32_e32 v56, v163
	v_mov_b32_e32 v57, v163
	v_mov_b32_e32 v58, v163
	v_mov_b32_e32 v59, v163
	v_mov_b32_e32 v60, v163
	v_mov_b32_e32 v61, v163
	v_mov_b32_e32 v62, v163
	v_mov_b32_e32 v63, v163
	v_mov_b32_e32 v64, v163
	v_mov_b32_e32 v65, v163
	v_mov_b32_e32 v82, 0
	v_mov_b32_e32 v83, v163
	v_mov_b32_e32 v84, v163
	v_mov_b32_e32 v85, v163
	v_mov_b32_e32 v86, v163
	v_mov_b32_e32 v87, v163
	v_mov_b32_e32 v88, v163
	v_mov_b32_e32 v89, v163
	v_mov_b32_e32 v90, v163
	v_mov_b32_e32 v91, v163
	v_mov_b32_e32 v92, v163
	v_mov_b32_e32 v93, v163
	v_mov_b32_e32 v94, v163
	v_mov_b32_e32 v95, v163
	v_mov_b32_e32 v96, v163
	v_mov_b32_e32 v97, v163
	v_mov_b32_e32 v66, 0
	v_mov_b32_e32 v67, v163
	v_mov_b32_e32 v68, v163
	v_mov_b32_e32 v69, v163
	v_mov_b32_e32 v70, v163
	v_mov_b32_e32 v71, v163
	v_mov_b32_e32 v72, v163
	v_mov_b32_e32 v73, v163
	v_mov_b32_e32 v74, v163
	v_mov_b32_e32 v75, v163
	v_mov_b32_e32 v76, v163
	v_mov_b32_e32 v77, v163
	v_mov_b32_e32 v78, v163
	v_mov_b32_e32 v79, v163
	v_mov_b32_e32 v80, v163
	v_mov_b32_e32 v81, v163
	v_mov_b32_e32 v98, 0
	v_mov_b32_e32 v99, v163
	v_mov_b32_e32 v100, v163
	v_mov_b32_e32 v101, v163
	v_mov_b32_e32 v102, v163
	v_mov_b32_e32 v103, v163
	v_mov_b32_e32 v104, v163
	v_mov_b32_e32 v105, v163
	v_mov_b32_e32 v106, v163
	v_mov_b32_e32 v107, v163
	v_mov_b32_e32 v108, v163
	v_mov_b32_e32 v109, v163
	v_mov_b32_e32 v110, v163
	v_mov_b32_e32 v111, v163
	v_mov_b32_e32 v112, v163
	v_mov_b32_e32 v113, v163
	v_mov_b32_e32 v114, 0
	v_mov_b32_e32 v115, v163
	v_mov_b32_e32 v116, v163
	v_mov_b32_e32 v117, v163
	v_mov_b32_e32 v118, v163
	v_mov_b32_e32 v119, v163
	v_mov_b32_e32 v120, v163
	v_mov_b32_e32 v121, v163
	v_mov_b32_e32 v122, v163
	v_mov_b32_e32 v123, v163
	v_mov_b32_e32 v124, v163
	v_mov_b32_e32 v125, v163
	v_mov_b32_e32 v126, v163
	v_mov_b32_e32 v127, v163
	v_mov_b32_e32 v128, v163
	v_mov_b32_e32 v129, v163
	v_readfirstlane_b32 s4, v208
	s_nop 3
	s_cmp_lg_u32 s4, 0
	s_cbranch_scc1 .LBB0_640
	s_mul_i32 s4, s79, 0x700
	s_add_i32 s4, s4, 0x20800
	v_lshl_add_u32 v250, v196, 2, s4
	ds_write_b32 v250, v162 offset:0
	ds_write_b32 v250, v164 offset:256
	ds_write_b32 v250, v166 offset:512
	ds_write_b32 v250, v168 offset:768
	ds_write_b32 v250, v170 offset:1024
	ds_write_b32 v250, v172 offset:1280
	ds_write_b32 v250, v174 offset:1536
	v_add_u32_e32 v178, s24, v180
	v_add_u32_e32 v179, s24, v182
	v_add_u32_e32 v181, s24, v184
	v_add_u32_e32 v183, s24, v186
	v_add_u32_e32 v251, s24, v188
	v_add_u32_e32 v174, s24, v190
	v_add_u32_e32 v175, s24, v192
	v_add_u32_e32 v203, s24, v194
	v_mov_b32_e32 v130, v196
	v_ashrrev_i32_e32 v131, 4, v130
	v_and_b32_e32 v132, 15, v130
	v_add_u32_e32 v136, s25, v131
	v_bitop3_b32 v137, v136, v132, 15 bitop3:0x6c
	v_mul_lo_u32 v136, v136, s44
	v_ashrrev_i32_e32 v133, 5, v130
	v_add_u32_e32 v136, s67, v136
	v_lshlrev_b32_e32 v137, 4, v137
	v_lshl_or_b32 v136, v136, 1, v137
	v_add_u32_e32 v137, s26, v133
	v_bfe_u32 v134, v130, 2, 3
	v_lshrrev_b32_e32 v135, 1, v130
	v_lshlrev_b32_e32 v138, 1, v137
	v_lshlrev_b32_e32 v135, 3, v130
	v_and_b32_e32 v138, 0xfffff0, v138
	v_and_b32_e32 v137, 4, v137
	v_lshlrev_b32_e32 v137, 1, v137
	v_and_b32_e32 v135, 24, v135
	v_or3_b32 v137, v137, v138, v134
	v_and_b32_e32 v130, 0x60, v130
	v_mul_u32_u24_e32 v137, 0x1900, v137
	v_or3_b32 v130, s69, v130, v135
	v_add_lshl_u32 v130, v130, v137, 1
	v_mov_b32_e32 v185, v136
	v_mov_b32_e32 v187, v130
	v_add_u32_e32 v130, s28, v131
	v_mul_lo_u32 v131, v130, s44
	v_bitop3_b32 v130, v130, v132, 15 bitop3:0x6c
	v_add_u32_e32 v131, s67, v131
	v_lshlrev_b32_e32 v130, 4, v130
	v_lshl_or_b32 v130, v131, 1, v130
	v_mov_b32_e32 v189, v130
	v_add_u32_e32 v131, s29, v133
	v_lshlrev_b32_e32 v132, 1, v131
	v_and_b32_e32 v132, 0xfffff0, v132
	v_and_b32_e32 v133, 4, v131
	v_lshlrev_b32_e32 v133, 1, v133
	v_lshlrev_b32_e32 v131, 5, v131
	v_or3_b32 v132, v133, v132, v134
	v_and_b32_e32 v131, 0x60, v131
	v_mul_u32_u24_e32 v132, 0x1900, v132
	v_or3_b32 v131, s69, v131, v135
	v_add_lshl_u32 v131, v131, v132, 1
	v_mov_b32_e32 v191, v131
	v_mov_b32_e32 v193, 0
	v_mov_b32_e32 v209, 0
	s_waitcnt lgkmcnt(0)

.Lfa_skip0:
	s_waitcnt lgkmcnt(10)
	v_mfma_f32_32x32x16_bf16 v[146:161], v[242:245], v[214:217], v[146:161]
	s_waitcnt lgkmcnt(9)
	v_mfma_f32_32x32x16_bf16 v[130:145], v[210:213], v[214:217], v[130:145]
	ds_read_b128 v[242:245], v190 offset:32768
	ds_read_b128 v[198:201], v174 offset:0
	ds_read_b128 v[246:249], v190 offset:40960
	s_waitcnt lgkmcnt(10)
	v_mfma_f32_32x32x16_bf16 v[146:161], v[218:221], v[226:229], v[146:161]
	s_waitcnt lgkmcnt(9)
	v_mfma_f32_32x32x16_bf16 v[130:145], v[222:225], v[226:229], v[130:145]
	s_waitcnt lgkmcnt(7)
	v_mfma_f32_32x32x16_bf16 v[146:161], v[230:233], v[238:241], v[146:161]
	s_waitcnt lgkmcnt(6)
	v_mfma_f32_32x32x16_bf16 v[130:145], v[234:237], v[238:241], v[130:145]
	s_waitcnt lgkmcnt(4)
	v_mfma_f32_32x32x16_bf16 v[210:225], v[162:165], v[170:173], 0
	s_waitcnt lgkmcnt(3)
	v_mfma_f32_32x32x16_bf16 v[226:241], v[166:169], v[170:173], 0
	ds_read_b128 v[162:165], v192 offset:32768
	ds_read_b128 v[170:173], v175 offset:0
	ds_read_b128 v[166:169], v192 offset:40960
	s_waitcnt lgkmcnt(4)
	v_mfma_f32_32x32x16_bf16 v[210:225], v[242:245], v[198:201], v[210:225]
	s_nop 0
	v_exp_f32_e32 v146, v146
	v_exp_f32_e32 v147, v147
	v_exp_f32_e32 v148, v148
	v_exp_f32_e32 v149, v149
	v_exp_f32_e32 v150, v150
	s_waitcnt lgkmcnt(3)
	v_mfma_f32_32x32x16_bf16 v[226:241], v[246:249], v[198:201], v[226:241]
	ds_read_b128 v[242:245], v194 offset:32768
	ds_read_b128 v[198:201], v203 offset:0
	ds_read_b128 v[246:249], v194 offset:40960
	v_exp_f32_e32 v151, v151
	v_exp_f32_e32 v152, v152
	v_exp_f32_e32 v153, v153
	v_add_f32_e32 v207, v207, v146
	v_add_f32_e32 v193, v193, v147
	s_waitcnt lgkmcnt(4)
	v_mfma_f32_32x32x16_bf16 v[210:225], v[162:165], v[170:173], v[210:225]
	v_add_f32_e32 v207, v207, v148
	v_add_f32_e32 v193, v193, v149
	v_add_f32_e32 v207, v207, v150
	v_add_f32_e32 v193, v193, v151
	v_add_f32_e32 v207, v207, v152
	s_waitcnt lgkmcnt(3)
	v_mfma_f32_32x32x16_bf16 v[226:241], v[166:169], v[170:173], v[226:241]
	v_add_f32_e32 v193, v193, v153
	v_cvt_pk_bf16_f32 v146, v146, v147
	v_cvt_pk_bf16_f32 v147, v148, v149
	v_cvt_pk_bf16_f32 v148, v150, v151
	v_cvt_pk_bf16_f32 v149, v152, v153
	ds_read_b64_tr_b16 v[162:163], v195 offset:0
	ds_read_b64_tr_b16 v[164:165], v195 offset:2048
	ds_read_b64_tr_b16 v[166:167], v195 offset:512
	ds_read_b64_tr_b16 v[168:169], v195 offset:2560
	ds_read_b64_tr_b16 v[170:171], v195 offset:1024
	ds_read_b64_tr_b16 v[172:173], v195 offset:3072
	s_waitcnt lgkmcnt(7)
	v_mfma_f32_32x32x16_bf16 v[210:225], v[242:245], v[198:201], v[210:225]
	s_waitcnt lgkmcnt(6)
	v_mfma_f32_32x32x16_bf16 v[226:241], v[246:249], v[198:201], v[226:241]
	ds_read_b64_tr_b16 v[242:243], v195 offset:1536
	ds_read_b64_tr_b16 v[244:245], v195 offset:3584
	ds_read_b64_tr_b16 v[246:247], v195 offset:4096
	ds_read_b64_tr_b16 v[248:249], v195 offset:6144
	ds_read_b64_tr_b16 v[198:199], v195 offset:4608
	ds_read_b64_tr_b16 v[200:201], v195 offset:6656
	s_nop 3
	v_exp_f32_e32 v210, v210
	v_exp_f32_e32 v211, v211
	v_exp_f32_e32 v212, v212
	v_exp_f32_e32 v213, v213
	v_exp_f32_e32 v214, v214
	v_exp_f32_e32 v215, v215
	v_exp_f32_e32 v216, v216
	v_exp_f32_e32 v217, v217
	v_add_f32_e32 v206, v206, v210
	v_add_f32_e32 v209, v209, v211
	v_add_f32_e32 v206, v206, v212
	v_add_f32_e32 v209, v209, v213
	v_add_f32_e32 v206, v206, v214
	v_add_f32_e32 v209, v209, v215
	v_add_f32_e32 v206, v206, v216
	v_add_f32_e32 v209, v209, v217
	v_cvt_pk_bf16_f32 v210, v210, v211
	v_cvt_pk_bf16_f32 v211, v212, v213
	v_cvt_pk_bf16_f32 v212, v214, v215
	v_cvt_pk_bf16_f32 v213, v216, v217
	s_waitcnt lgkmcnt(10)
	v_mfma_f32_32x32x16_bf16 v[82:97], v[146:149], v[162:165], v[82:97]
	v_exp_f32_e32 v154, v154
	v_exp_f32_e32 v155, v155
	v_exp_f32_e32 v156, v156
	v_exp_f32_e32 v157, v157
	v_exp_f32_e32 v158, v158
	v_mfma_f32_32x32x16_bf16 v[50:65], v[210:213], v[162:165], v[50:65]
	v_exp_f32_e32 v159, v159
	v_exp_f32_e32 v160, v160
	v_exp_f32_e32 v161, v161
	v_add_f32_e32 v207, v207, v154
	v_add_f32_e32 v193, v193, v155
	ds_read_b64_tr_b16 v[162:163], v195 offset:5120
	ds_read_b64_tr_b16 v[164:165], v195 offset:7168
	s_waitcnt lgkmcnt(10)
	v_mfma_f32_32x32x16_bf16 v[66:81], v[146:149], v[166:169], v[66:81]
	v_add_f32_e32 v207, v207, v156
	v_add_f32_e32 v193, v193, v157
	v_add_f32_e32 v207, v207, v158
	v_add_f32_e32 v193, v193, v159
	v_add_f32_e32 v207, v207, v160
	v_mfma_f32_32x32x16_bf16 v[34:49], v[210:213], v[166:169], v[34:49]
	v_add_f32_e32 v193, v193, v161
	v_cvt_pk_bf16_f32 v154, v154, v155
	v_cvt_pk_bf16_f32 v155, v156, v157
	v_cvt_pk_bf16_f32 v156, v158, v159
	v_cvt_pk_bf16_f32 v157, v160, v161
	ds_read_b64_tr_b16 v[166:167], v195 offset:5632
	ds_read_b64_tr_b16 v[168:169], v195 offset:7680
	s_waitcnt lgkmcnt(10)
	v_mfma_f32_32x32x16_bf16 v[98:113], v[146:149], v[170:173], v[98:113]
	v_exp_f32_e32 v218, v218
	v_exp_f32_e32 v219, v219
	v_exp_f32_e32 v220, v220
	v_exp_f32_e32 v221, v221
	v_exp_f32_e32 v222, v222
	v_mfma_f32_32x32x16_bf16 v[18:33], v[210:213], v[170:173], v[18:33]
	v_exp_f32_e32 v223, v223
	v_exp_f32_e32 v224, v224
	v_exp_f32_e32 v225, v225
	v_add_f32_e32 v206, v206, v218
	v_add_f32_e32 v209, v209, v219
	ds_read_b64_tr_b16 v[170:171], v195 offset:8192
	ds_read_b64_tr_b16 v[172:173], v195 offset:10240
	s_waitcnt lgkmcnt(10)
	v_mfma_f32_32x32x16_bf16 v[114:129], v[146:149], v[242:245], v[114:129]
	v_add_f32_e32 v206, v206, v220
	v_add_f32_e32 v209, v209, v221
	v_add_f32_e32 v206, v206, v222
	v_add_f32_e32 v209, v209, v223
	v_add_f32_e32 v206, v206, v224
	v_mfma_f32_32x32x16_bf16 v[2:17], v[210:213], v[242:245], v[2:17]
	v_add_f32_e32 v209, v209, v225
	v_cvt_pk_bf16_f32 v218, v218, v219
	v_cvt_pk_bf16_f32 v219, v220, v221
	v_cvt_pk_bf16_f32 v220, v222, v223
	v_cvt_pk_bf16_f32 v221, v224, v225
	ds_read_b64_tr_b16 v[242:243], v195 offset:8704
	ds_read_b64_tr_b16 v[244:245], v195 offset:10752
	s_waitcnt lgkmcnt(10)
	v_mfma_f32_32x32x16_bf16 v[82:97], v[154:157], v[246:249], v[82:97]
	v_exp_f32_e32 v130, v130
	v_exp_f32_e32 v131, v131
	v_exp_f32_e32 v132, v132
	v_exp_f32_e32 v133, v133
	v_exp_f32_e32 v134, v134
	v_mfma_f32_32x32x16_bf16 v[50:65], v[218:221], v[246:249], v[50:65]
	v_exp_f32_e32 v135, v135
	v_exp_f32_e32 v136, v136
	v_exp_f32_e32 v137, v137
	v_add_f32_e32 v207, v207, v130
	v_add_f32_e32 v193, v193, v131
	ds_read_b64_tr_b16 v[246:247], v195 offset:9216
	ds_read_b64_tr_b16 v[248:249], v195 offset:11264
	s_waitcnt lgkmcnt(10)
	v_mfma_f32_32x32x16_bf16 v[66:81], v[154:157], v[198:201], v[66:81]
	v_add_f32_e32 v207, v207, v132
	v_add_f32_e32 v193, v193, v133
	v_add_f32_e32 v207, v207, v134
	v_add_f32_e32 v193, v193, v135
	v_add_f32_e32 v207, v207, v136
	v_mfma_f32_32x32x16_bf16 v[34:49], v[218:221], v[198:201], v[34:49]
	v_add_f32_e32 v193, v193, v137
	v_cvt_pk_bf16_f32 v130, v130, v131
	v_cvt_pk_bf16_f32 v131, v132, v133
	v_cvt_pk_bf16_f32 v132, v134, v135
	v_cvt_pk_bf16_f32 v133, v136, v137
	ds_read_b64_tr_b16 v[198:199], v195 offset:9728
	ds_read_b64_tr_b16 v[200:201], v195 offset:11776
	s_waitcnt lgkmcnt(10)
	v_mfma_f32_32x32x16_bf16 v[98:113], v[154:157], v[162:165], v[98:113]
	v_exp_f32_e32 v226, v226
	v_exp_f32_e32 v227, v227
	v_exp_f32_e32 v228, v228
	v_exp_f32_e32 v229, v229
	v_exp_f32_e32 v230, v230
	v_mfma_f32_32x32x16_bf16 v[18:33], v[218:221], v[162:165], v[18:33]
	v_exp_f32_e32 v231, v231
	v_exp_f32_e32 v232, v232
	v_exp_f32_e32 v233, v233
	v_add_f32_e32 v206, v206, v226
	v_add_f32_e32 v209, v209, v227
	ds_read_b64_tr_b16 v[162:163], v195 offset:12288
	ds_read_b64_tr_b16 v[164:165], v195 offset:14336
	s_waitcnt lgkmcnt(10)
	v_mfma_f32_32x32x16_bf16 v[114:129], v[154:157], v[166:169], v[114:129]
	v_add_f32_e32 v206, v206, v228
	v_add_f32_e32 v209, v209, v229
	v_add_f32_e32 v206, v206, v230
	v_add_f32_e32 v209, v209, v231
	v_add_f32_e32 v206, v206, v232
	v_mfma_f32_32x32x16_bf16 v[2:17], v[218:221], v[166:169], v[2:17]
	v_add_f32_e32 v209, v209, v233
	v_cvt_pk_bf16_f32 v226, v226, v227
	v_cvt_pk_bf16_f32 v227, v228, v229
	v_cvt_pk_bf16_f32 v228, v230, v231
	v_cvt_pk_bf16_f32 v229, v232, v233
	ds_read_b64_tr_b16 v[166:167], v195 offset:12800
	ds_read_b64_tr_b16 v[168:169], v195 offset:14848
	s_waitcnt lgkmcnt(10)
	v_mfma_f32_32x32x16_bf16 v[82:97], v[130:133], v[170:173], v[82:97]
	v_exp_f32_e32 v138, v138
	v_exp_f32_e32 v139, v139
	v_exp_f32_e32 v140, v140
	v_exp_f32_e32 v141, v141
	v_exp_f32_e32 v142, v142
	v_mfma_f32_32x32x16_bf16 v[50:65], v[226:229], v[170:173], v[50:65]
	v_exp_f32_e32 v143, v143
	v_exp_f32_e32 v144, v144
	v_exp_f32_e32 v145, v145
	v_add_f32_e32 v207, v207, v138
	v_add_f32_e32 v193, v193, v139
	ds_read_b64_tr_b16 v[170:171], v195 offset:13312
	ds_read_b64_tr_b16 v[172:173], v195 offset:15360
	s_waitcnt lgkmcnt(10)
	v_mfma_f32_32x32x16_bf16 v[66:81], v[130:133], v[242:245], v[66:81]
	v_add_f32_e32 v207, v207, v140
	v_add_f32_e32 v193, v193, v141
	v_add_f32_e32 v207, v207, v142
	v_add_f32_e32 v193, v193, v143
	v_add_f32_e32 v207, v207, v144
	v_mfma_f32_32x32x16_bf16 v[34:49], v[226:229], v[242:245], v[34:49]
	v_add_f32_e32 v193, v193, v145
	v_cvt_pk_bf16_f32 v138, v138, v139
	v_cvt_pk_bf16_f32 v139, v140, v141
	v_cvt_pk_bf16_f32 v140, v142, v143
	v_cvt_pk_bf16_f32 v141, v144, v145
	ds_read_b64_tr_b16 v[242:243], v195 offset:13824
	ds_read_b64_tr_b16 v[244:245], v195 offset:15872
	s_waitcnt lgkmcnt(10)
	v_mfma_f32_32x32x16_bf16 v[98:113], v[130:133], v[246:249], v[98:113]
	v_exp_f32_e32 v234, v234
	v_exp_f32_e32 v235, v235
	v_exp_f32_e32 v236, v236
	v_exp_f32_e32 v237, v237
	v_exp_f32_e32 v238, v238
	v_mfma_f32_32x32x16_bf16 v[18:33], v[226:229], v[246:249], v[18:33]
	v_exp_f32_e32 v239, v239
	v_exp_f32_e32 v240, v240
	v_exp_f32_e32 v241, v241
	v_add_f32_e32 v206, v206, v234
	v_add_f32_e32 v209, v209, v235
	s_waitcnt lgkmcnt(8)
	v_mfma_f32_32x32x16_bf16 v[114:129], v[130:133], v[198:201], v[114:129]
	v_add_f32_e32 v206, v206, v236
	v_add_f32_e32 v209, v209, v237
	v_add_f32_e32 v206, v206, v238
	v_add_f32_e32 v209, v209, v239
	v_add_f32_e32 v206, v206, v240
	v_mfma_f32_32x32x16_bf16 v[2:17], v[226:229], v[198:201], v[2:17]
	v_add_f32_e32 v209, v209, v241
	v_cvt_pk_bf16_f32 v234, v234, v235
	v_cvt_pk_bf16_f32 v235, v236, v237
	v_cvt_pk_bf16_f32 v236, v238, v239
	v_cvt_pk_bf16_f32 v237, v240, v241
	s_waitcnt lgkmcnt(6)
	v_mfma_f32_32x32x16_bf16 v[82:97], v[138:141], v[162:165], v[82:97]
	v_mfma_f32_32x32x16_bf16 v[50:65], v[234:237], v[162:165], v[50:65]
	s_waitcnt lgkmcnt(4)
	v_mfma_f32_32x32x16_bf16 v[66:81], v[138:141], v[166:169], v[66:81]
	v_mfma_f32_32x32x16_bf16 v[34:49], v[234:237], v[166:169], v[34:49]
	s_waitcnt lgkmcnt(2)
	v_mfma_f32_32x32x16_bf16 v[98:113], v[138:141], v[170:173], v[98:113]
	v_mfma_f32_32x32x16_bf16 v[18:33], v[234:237], v[170:173], v[18:33]
	s_waitcnt lgkmcnt(0)
	v_mfma_f32_32x32x16_bf16 v[114:129], v[138:141], v[242:245], v[114:129]
	v_mfma_f32_32x32x16_bf16 v[2:17], v[234:237], v[242:245], v[2:17]
	s_add_i32 s72, s72, 1
	s_add_i32 s71, s71, 64
	s_addk_i32 s70, 0x4000
	s_waitcnt vmcnt(0)
	s_barrier
	ds_read_b128 v[162:165], v180 offset:49152
	ds_read_b128 v[170:173], v178 offset:0
	ds_read_b128 v[166:169], v180 offset:57344
	ds_read_b128 v[242:245], v182 offset:49152
	ds_read_b128 v[214:217], v179 offset:0
	ds_read_b128 v[210:213], v182 offset:57344
	ds_read_b128 v[218:221], v184 offset:49152
	ds_read_b128 v[226:229], v181 offset:0
	ds_read_b128 v[222:225], v184 offset:57344
	ds_read_b128 v[230:233], v186 offset:49152
	ds_read_b128 v[238:241], v183 offset:0
	ds_read_b128 v[234:237], v186 offset:57344
	s_waitcnt lgkmcnt(10)
	v_mfma_f32_32x32x16_bf16 v[146:161], v[162:165], v[170:173], 0
	s_waitcnt lgkmcnt(9)
	v_mfma_f32_32x32x16_bf16 v[130:145], v[166:169], v[170:173], 0
	ds_read_b128 v[162:165], v188 offset:49152
	ds_read_b128 v[170:173], v251 offset:0
	ds_read_b128 v[166:169], v188 offset:57344
	s_cmpk_eq_i32 s72, 0x43
	s_cbranch_scc1 .Lfa_skip1
	s_cmp_lt_u32 s72, 3
	s_cselect_b32 s5, s66, s68
	s_add_i32 s5, s5, s71
	s_mul_hi_i32 s19, s5, 0x3200
	s_mulk_i32 s5, 0x3200
	s_add_u32 s18, s20, s5
	s_addc_u32 s19, s21, s19
	s_add_i32 s75, s27, 0x0
	s_add_i32 s5, s30, 0x0
	s_add_i32 m0, s75, 0x8000
	s_nop 0
	global_load_lds_dwordx4 v185, s[18:19]
	s_mov_b32 m0, s75
	s_nop 0
	global_load_lds_dwordx4 v187, s[18:19]
	s_add_i32 m0, s5, 0x8000
	s_nop 0
	global_load_lds_dwordx4 v189, s[18:19]
	s_mov_b32 m0, s5
	s_nop 0
	global_load_lds_dwordx4 v191, s[18:19]
.Lfa_skip1:
	s_waitcnt lgkmcnt(10)
	v_mfma_f32_32x32x16_bf16 v[146:161], v[242:245], v[214:217], v[146:161]
	s_waitcnt lgkmcnt(9)
	v_mfma_f32_32x32x16_bf16 v[130:145], v[210:213], v[214:217], v[130:145]
	ds_read_b128 v[242:245], v190 offset:49152
	ds_read_b128 v[198:201], v174 offset:0
	ds_read_b128 v[246:249], v190 offset:57344
	s_waitcnt lgkmcnt(10)
	v_mfma_f32_32x32x16_bf16 v[146:161], v[218:221], v[226:229], v[146:161]
	s_waitcnt lgkmcnt(9)
	v_mfma_f32_32x32x16_bf16 v[130:145], v[222:225], v[226:229], v[130:145]
	s_waitcnt lgkmcnt(7)
	v_mfma_f32_32x32x16_bf16 v[146:161], v[230:233], v[238:241], v[146:161]
	s_waitcnt lgkmcnt(6)
	v_mfma_f32_32x32x16_bf16 v[130:145], v[234:237], v[238:241], v[130:145]
	s_waitcnt lgkmcnt(4)
	v_mfma_f32_32x32x16_bf16 v[210:225], v[162:165], v[170:173], 0
	s_waitcnt lgkmcnt(3)
	v_mfma_f32_32x32x16_bf16 v[226:241], v[166:169], v[170:173], 0
	ds_read_b128 v[162:165], v192 offset:49152
	ds_read_b128 v[170:173], v175 offset:0
	ds_read_b128 v[166:169], v192 offset:57344
	s_waitcnt lgkmcnt(4)
	v_mfma_f32_32x32x16_bf16 v[210:225], v[242:245], v[198:201], v[210:225]
	s_nop 0
	v_exp_f32_e32 v146, v146
	v_exp_f32_e32 v147, v147
	v_exp_f32_e32 v148, v148
	v_exp_f32_e32 v149, v149
	v_exp_f32_e32 v150, v150
	s_waitcnt lgkmcnt(3)
	v_mfma_f32_32x32x16_bf16 v[226:241], v[246:249], v[198:201], v[226:241]
	ds_read_b128 v[242:245], v194 offset:49152
	ds_read_b128 v[198:201], v203 offset:0
	ds_read_b128 v[246:249], v194 offset:57344
	v_exp_f32_e32 v151, v151
	v_exp_f32_e32 v152, v152
	v_exp_f32_e32 v153, v153
	v_add_f32_e32 v207, v207, v146
	v_add_f32_e32 v193, v193, v147
	s_waitcnt lgkmcnt(4)
	v_mfma_f32_32x32x16_bf16 v[210:225], v[162:165], v[170:173], v[210:225]
	v_add_f32_e32 v207, v207, v148
	v_add_f32_e32 v193, v193, v149
	v_add_f32_e32 v207, v207, v150
	v_add_f32_e32 v193, v193, v151
	v_add_f32_e32 v207, v207, v152
	s_waitcnt lgkmcnt(3)
	v_mfma_f32_32x32x16_bf16 v[226:241], v[166:169], v[170:173], v[226:241]
	v_add_f32_e32 v193, v193, v153
	v_cvt_pk_bf16_f32 v146, v146, v147
	v_cvt_pk_bf16_f32 v147, v148, v149
	v_cvt_pk_bf16_f32 v148, v150, v151
	v_cvt_pk_bf16_f32 v149, v152, v153
	ds_read_b64_tr_b16 v[162:163], v195 offset:16384
	ds_read_b64_tr_b16 v[164:165], v195 offset:18432
	ds_read_b64_tr_b16 v[166:167], v195 offset:16896
	ds_read_b64_tr_b16 v[168:169], v195 offset:18944
	ds_read_b64_tr_b16 v[170:171], v195 offset:17408
	ds_read_b64_tr_b16 v[172:173], v195 offset:19456
	s_waitcnt lgkmcnt(7)
	v_mfma_f32_32x32x16_bf16 v[210:225], v[242:245], v[198:201], v[210:225]
	s_waitcnt lgkmcnt(6)
	v_mfma_f32_32x32x16_bf16 v[226:241], v[246:249], v[198:201], v[226:241]
	ds_read_b64_tr_b16 v[242:243], v195 offset:17920
	ds_read_b64_tr_b16 v[244:245], v195 offset:19968
	ds_read_b64_tr_b16 v[246:247], v195 offset:20480
	ds_read_b64_tr_b16 v[248:249], v195 offset:22528
	ds_read_b64_tr_b16 v[198:199], v195 offset:20992
	ds_read_b64_tr_b16 v[200:201], v195 offset:23040
	s_nop 3
	v_exp_f32_e32 v210, v210
	v_exp_f32_e32 v211, v211
	v_exp_f32_e32 v212, v212
	v_exp_f32_e32 v213, v213
	v_exp_f32_e32 v214, v214
	v_exp_f32_e32 v215, v215
	v_exp_f32_e32 v216, v216
	v_exp_f32_e32 v217, v217
	v_add_f32_e32 v206, v206, v210
	v_add_f32_e32 v209, v209, v211
	v_add_f32_e32 v206, v206, v212
	v_add_f32_e32 v209, v209, v213
	v_add_f32_e32 v206, v206, v214
	v_add_f32_e32 v209, v209, v215
	v_add_f32_e32 v206, v206, v216
	v_add_f32_e32 v209, v209, v217
	v_cvt_pk_bf16_f32 v210, v210, v211
	v_cvt_pk_bf16_f32 v211, v212, v213
	v_cvt_pk_bf16_f32 v212, v214, v215
	v_cvt_pk_bf16_f32 v213, v216, v217
	s_waitcnt lgkmcnt(10)
	v_mfma_f32_32x32x16_bf16 v[82:97], v[146:149], v[162:165], v[82:97]
	v_exp_f32_e32 v154, v154
	v_exp_f32_e32 v155, v155
	v_exp_f32_e32 v156, v156
	v_exp_f32_e32 v157, v157
	v_exp_f32_e32 v158, v158
	v_mfma_f32_32x32x16_bf16 v[50:65], v[210:213], v[162:165], v[50:65]
	v_exp_f32_e32 v159, v159
	v_exp_f32_e32 v160, v160
	v_exp_f32_e32 v161, v161
	v_add_f32_e32 v207, v207, v154
	v_add_f32_e32 v193, v193, v155
	ds_read_b64_tr_b16 v[162:163], v195 offset:21504
	ds_read_b64_tr_b16 v[164:165], v195 offset:23552
	s_waitcnt lgkmcnt(10)
	v_mfma_f32_32x32x16_bf16 v[66:81], v[146:149], v[166:169], v[66:81]
	v_add_f32_e32 v207, v207, v156
	v_add_f32_e32 v193, v193, v157
	v_add_f32_e32 v207, v207, v158
	v_add_f32_e32 v193, v193, v159
	v_add_f32_e32 v207, v207, v160
	v_mfma_f32_32x32x16_bf16 v[34:49], v[210:213], v[166:169], v[34:49]
	v_add_f32_e32 v193, v193, v161
	v_cvt_pk_bf16_f32 v154, v154, v155
	v_cvt_pk_bf16_f32 v155, v156, v157
	v_cvt_pk_bf16_f32 v156, v158, v159
	v_cvt_pk_bf16_f32 v157, v160, v161
	ds_read_b64_tr_b16 v[166:167], v195 offset:22016
	ds_read_b64_tr_b16 v[168:169], v195 offset:24064
	s_waitcnt lgkmcnt(10)
	v_mfma_f32_32x32x16_bf16 v[98:113], v[146:149], v[170:173], v[98:113]
	v_exp_f32_e32 v218, v218
	v_exp_f32_e32 v219, v219
	v_exp_f32_e32 v220, v220
	v_exp_f32_e32 v221, v221
	v_exp_f32_e32 v222, v222
	v_mfma_f32_32x32x16_bf16 v[18:33], v[210:213], v[170:173], v[18:33]
	v_exp_f32_e32 v223, v223
	v_exp_f32_e32 v224, v224
	v_exp_f32_e32 v225, v225
	v_add_f32_e32 v206, v206, v218
	v_add_f32_e32 v209, v209, v219
	ds_read_b64_tr_b16 v[170:171], v195 offset:24576
	ds_read_b64_tr_b16 v[172:173], v195 offset:26624
	s_waitcnt lgkmcnt(10)
	v_mfma_f32_32x32x16_bf16 v[114:129], v[146:149], v[242:245], v[114:129]
	v_add_f32_e32 v206, v206, v220
	v_add_f32_e32 v209, v209, v221
	v_add_f32_e32 v206, v206, v222
	v_add_f32_e32 v209, v209, v223
	v_add_f32_e32 v206, v206, v224
	v_mfma_f32_32x32x16_bf16 v[2:17], v[210:213], v[242:245], v[2:17]
	v_add_f32_e32 v209, v209, v225
	v_cvt_pk_bf16_f32 v218, v218, v219
	v_cvt_pk_bf16_f32 v219, v220, v221
	v_cvt_pk_bf16_f32 v220, v222, v223
	v_cvt_pk_bf16_f32 v221, v224, v225
	ds_read_b64_tr_b16 v[242:243], v195 offset:25088
	ds_read_b64_tr_b16 v[244:245], v195 offset:27136
	s_waitcnt lgkmcnt(10)
	v_mfma_f32_32x32x16_bf16 v[82:97], v[154:157], v[246:249], v[82:97]
	v_exp_f32_e32 v130, v130
	v_exp_f32_e32 v131, v131
	v_exp_f32_e32 v132, v132
	v_exp_f32_e32 v133, v133
	v_exp_f32_e32 v134, v134
	v_mfma_f32_32x32x16_bf16 v[50:65], v[218:221], v[246:249], v[50:65]
	v_exp_f32_e32 v135, v135
	v_exp_f32_e32 v136, v136
	v_exp_f32_e32 v137, v137
	v_add_f32_e32 v207, v207, v130
	v_add_f32_e32 v193, v193, v131
	ds_read_b64_tr_b16 v[246:247], v195 offset:25600
	ds_read_b64_tr_b16 v[248:249], v195 offset:27648
	s_waitcnt lgkmcnt(10)
	v_mfma_f32_32x32x16_bf16 v[66:81], v[154:157], v[198:201], v[66:81]
	v_add_f32_e32 v207, v207, v132
	v_add_f32_e32 v193, v193, v133
	v_add_f32_e32 v207, v207, v134
	v_add_f32_e32 v193, v193, v135
	v_add_f32_e32 v207, v207, v136
	v_mfma_f32_32x32x16_bf16 v[34:49], v[218:221], v[198:201], v[34:49]
	v_add_f32_e32 v193, v193, v137
	v_cvt_pk_bf16_f32 v130, v130, v131
	v_cvt_pk_bf16_f32 v131, v132, v133
	v_cvt_pk_bf16_f32 v132, v134, v135
	v_cvt_pk_bf16_f32 v133, v136, v137
	ds_read_b64_tr_b16 v[198:199], v195 offset:26112
	ds_read_b64_tr_b16 v[200:201], v195 offset:28160
	s_waitcnt lgkmcnt(10)
	v_mfma_f32_32x32x16_bf16 v[98:113], v[154:157], v[162:165], v[98:113]
	v_exp_f32_e32 v226, v226
	v_exp_f32_e32 v227, v227
	v_exp_f32_e32 v228, v228
	v_exp_f32_e32 v229, v229
	v_exp_f32_e32 v230, v230
	v_mfma_f32_32x32x16_bf16 v[18:33], v[218:221], v[162:165], v[18:33]
	v_exp_f32_e32 v231, v231
	v_exp_f32_e32 v232, v232
	v_exp_f32_e32 v233, v233
	v_add_f32_e32 v206, v206, v226
	v_add_f32_e32 v209, v209, v227
	ds_read_b64_tr_b16 v[162:163], v195 offset:28672
	ds_read_b64_tr_b16 v[164:165], v195 offset:30720
	s_waitcnt lgkmcnt(10)
	v_mfma_f32_32x32x16_bf16 v[114:129], v[154:157], v[166:169], v[114:129]
	v_add_f32_e32 v206, v206, v228
	v_add_f32_e32 v209, v209, v229
	v_add_f32_e32 v206, v206, v230
	v_add_f32_e32 v209, v209, v231
	v_add_f32_e32 v206, v206, v232
	v_mfma_f32_32x32x16_bf16 v[2:17], v[218:221], v[166:169], v[2:17]
	v_add_f32_e32 v209, v209, v233
	v_cvt_pk_bf16_f32 v226, v226, v227
	v_cvt_pk_bf16_f32 v227, v228, v229
	v_cvt_pk_bf16_f32 v228, v230, v231
	v_cvt_pk_bf16_f32 v229, v232, v233
	ds_read_b64_tr_b16 v[166:167], v195 offset:29184
	ds_read_b64_tr_b16 v[168:169], v195 offset:31232
	s_waitcnt lgkmcnt(10)
	v_mfma_f32_32x32x16_bf16 v[82:97], v[130:133], v[170:173], v[82:97]
	v_exp_f32_e32 v138, v138
	v_exp_f32_e32 v139, v139
	v_exp_f32_e32 v140, v140
	v_exp_f32_e32 v141, v141
	v_exp_f32_e32 v142, v142
	v_mfma_f32_32x32x16_bf16 v[50:65], v[226:229], v[170:173], v[50:65]
	v_exp_f32_e32 v143, v143
	v_exp_f32_e32 v144, v144
	v_exp_f32_e32 v145, v145
	v_add_f32_e32 v207, v207, v138
	v_add_f32_e32 v193, v193, v139
	ds_read_b64_tr_b16 v[170:171], v195 offset:29696
	ds_read_b64_tr_b16 v[172:173], v195 offset:31744
	s_waitcnt lgkmcnt(10)
	v_mfma_f32_32x32x16_bf16 v[66:81], v[130:133], v[242:245], v[66:81]
	v_add_f32_e32 v207, v207, v140
	v_add_f32_e32 v193, v193, v141
	v_add_f32_e32 v207, v207, v142
	v_add_f32_e32 v193, v193, v143
	v_add_f32_e32 v207, v207, v144
	v_mfma_f32_32x32x16_bf16 v[34:49], v[226:229], v[242:245], v[34:49]
	v_add_f32_e32 v193, v193, v145
	v_cvt_pk_bf16_f32 v138, v138, v139
	v_cvt_pk_bf16_f32 v139, v140, v141
	v_cvt_pk_bf16_f32 v140, v142, v143
	v_cvt_pk_bf16_f32 v141, v144, v145
	ds_read_b64_tr_b16 v[242:243], v195 offset:30208
	ds_read_b64_tr_b16 v[244:245], v195 offset:32256
	s_waitcnt lgkmcnt(10)
	v_mfma_f32_32x32x16_bf16 v[98:113], v[130:133], v[246:249], v[98:113]
	v_exp_f32_e32 v234, v234
	v_exp_f32_e32 v235, v235
	v_exp_f32_e32 v236, v236
	v_exp_f32_e32 v237, v237
	v_exp_f32_e32 v238, v238
	v_mfma_f32_32x32x16_bf16 v[18:33], v[226:229], v[246:249], v[18:33]
	v_exp_f32_e32 v239, v239
	v_exp_f32_e32 v240, v240
	v_exp_f32_e32 v241, v241
	v_add_f32_e32 v206, v206, v234
	v_add_f32_e32 v209, v209, v235
	s_waitcnt lgkmcnt(8)
	v_mfma_f32_32x32x16_bf16 v[114:129], v[130:133], v[198:201], v[114:129]
	v_add_f32_e32 v206, v206, v236
	v_add_f32_e32 v209, v209, v237
	v_add_f32_e32 v206, v206, v238
	v_add_f32_e32 v209, v209, v239
	v_add_f32_e32 v206, v206, v240
	v_mfma_f32_32x32x16_bf16 v[2:17], v[226:229], v[198:201], v[2:17]
	v_add_f32_e32 v209, v209, v241
	v_cvt_pk_bf16_f32 v234, v234, v235
	v_cvt_pk_bf16_f32 v235, v236, v237
	v_cvt_pk_bf16_f32 v236, v238, v239
	v_cvt_pk_bf16_f32 v237, v240, v241
	s_waitcnt lgkmcnt(6)
	v_mfma_f32_32x32x16_bf16 v[82:97], v[138:141], v[162:165], v[82:97]
	v_mfma_f32_32x32x16_bf16 v[50:65], v[234:237], v[162:165], v[50:65]
	s_waitcnt lgkmcnt(4)
	v_mfma_f32_32x32x16_bf16 v[66:81], v[138:141], v[166:169], v[66:81]
	v_mfma_f32_32x32x16_bf16 v[34:49], v[234:237], v[166:169], v[34:49]
	s_waitcnt lgkmcnt(2)
	v_mfma_f32_32x32x16_bf16 v[98:113], v[138:141], v[170:173], v[98:113]
	v_mfma_f32_32x32x16_bf16 v[18:33], v[234:237], v[170:173], v[18:33]
	s_waitcnt lgkmcnt(0)
	v_mfma_f32_32x32x16_bf16 v[114:129], v[138:141], v[242:245], v[114:129]
	v_mfma_f32_32x32x16_bf16 v[2:17], v[234:237], v[242:245], v[2:17]
	s_add_i32 s72, s72, 1
	s_add_i32 s71, s71, 64
	s_addk_i32 s70, 0x4000
	s_cmpk_eq_i32 s72, 0x44
	s_waitcnt vmcnt(0)
	s_barrier
	s_cbranch_scc0 .Lfa_loop
	v_add_f32_e32 v207, v207, v193
	v_add_f32_e32 v206, v206, v209
	s_mul_i32 s4, s79, 0x700
	s_add_i32 s4, s4, 0x20800
	v_lshl_add_u32 v250, v196, 2, s4
	ds_read_b32 v162, v250 offset:0
	ds_read_b32 v164, v250 offset:256
	ds_read_b32 v166, v250 offset:512
	ds_read_b32 v168, v250 offset:768
	ds_read_b32 v170, v250 offset:1024
	ds_read_b32 v172, v250 offset:1280
	ds_read_b32 v174, v250 offset:1536
	v_mov_b32_e32 v163, 0
	v_mov_b32_e32 v165, 0
	v_mov_b32_e32 v167, 0
	v_mov_b32_e32 v169, 0
	v_mov_b32_e32 v171, 0
	v_mov_b32_e32 v173, 0
	v_mov_b32_e32 v175, 0
	v_lshlrev_b32_e32 v178, 8, v176
	v_mov_b32_e32 v198, 0x2800
	v_mov_b32_e32 v199, 0x8000
	v_mov_b32_e32 v200, 0x260
	v_mov_b32_e32 v201, 0xc2700000
	v_sub_u32_e32 v179, v180, v178
	v_sub_u32_e32 v181, v182, v178
	v_sub_u32_e32 v183, v184, v178
	v_sub_u32_e32 v185, v186, v178
	v_sub_u32_e32 v187, v188, v178
	v_sub_u32_e32 v189, v190, v178
	v_sub_u32_e32 v191, v192, v178
	v_sub_u32_e32 v193, v194, v178
	v_mov_b32_e32 v203, 0x358637bd
	s_waitcnt lgkmcnt(0)
	s_branch .LBB0_651
.LBB0_640:
	v_mov_b32_e32 v130, v208
	s_nop 0
	v_readfirstlane_b32 s4, v130
	s_setprio 1
	s_and_b32 s74, s70, 0x4000
	s_add_i32 s73, s74, 0
	v_add_u32_e32 v130, s73, v180
	ds_read_b128 v[130:133], v130 offset:32768
	v_add_u32_e32 v134, s24, v180
	ds_read_b128 v[134:137], v134
	v_add3_u32 v138, s73, v179, v178
	v_add_u32_e32 v209, s24, v182
	v_add_u32_e32 v142, s73, v182
	ds_read_b128 v[138:141], v138 offset:40960
	ds_read_b128 v[210:213], v142 offset:32768
	ds_read_b128 v[214:217], v209
	v_add3_u32 v209, s73, v181, v178
	s_waitcnt lgkmcnt(3)
	v_mfma_f32_32x32x16_bf16 v[146:161], v[130:133], v[134:137], 0
	s_waitcnt lgkmcnt(0)
	v_mfma_f32_32x32x16_bf16 v[146:161], v[210:213], v[214:217], v[146:161]
	ds_read_b128 v[210:213], v209 offset:40960
	v_add_u32_e32 v209, s73, v184
	v_mfma_f32_32x32x16_bf16 v[130:145], v[138:141], v[134:137], 0
	s_waitcnt lgkmcnt(0)
	v_mfma_f32_32x32x16_bf16 v[130:145], v[210:213], v[214:217], v[130:145]
	ds_read_b128 v[210:213], v209 offset:32768
	v_add_u32_e32 v209, s24, v184
	ds_read_b128 v[214:217], v209
	v_add3_u32 v209, s73, v183, v178
	ds_read_b128 v[218:221], v209 offset:40960
	v_add_u32_e32 v209, s73, v186
	ds_read_b128 v[222:225], v209 offset:32768
	v_add_u32_e32 v209, s24, v186
	s_waitcnt lgkmcnt(2)
	v_mfma_f32_32x32x16_bf16 v[146:161], v[210:213], v[214:217], v[146:161]
	ds_read_b128 v[210:213], v209
	v_add3_u32 v209, s73, v185, v178
	s_waitcnt lgkmcnt(2)
	v_mfma_f32_32x32x16_bf16 v[130:145], v[218:221], v[214:217], v[130:145]
	ds_read_b128 v[214:217], v209 offset:40960
	s_waitcnt lgkmcnt(1)
	v_mfma_f32_32x32x16_bf16 v[146:161], v[222:225], v[210:213], v[146:161]
	s_waitcnt lgkmcnt(0)
	v_mfma_f32_32x32x16_bf16 v[130:145], v[214:217], v[210:213], v[130:145]
	s_setprio 0
	s_cmpk_eq_i32 s72, 0x43
	s_cbranch_scc1 .LBB0_642
	v_mov_b32_e32 v209, v196
	s_cmp_lt_u32 s72, 3
	s_cselect_b32 s5, s66, s68
	v_ashrrev_i32_e32 v210, 4, v209
	v_and_b32_e32 v211, 15, v209
	v_add_u32_e32 v215, s25, v210
	s_add_i32 s5, s5, s71
	v_bitop3_b32 v216, v215, v211, 15 bitop3:0x6c
	v_mul_lo_u32 v215, v215, s44
	s_mul_hi_i32 s19, s5, 0x3200
	s_mulk_i32 s5, 0x3200
	v_ashrrev_i32_e32 v212, 5, v209
	v_add_u32_e32 v215, s67, v215
	v_lshlrev_b32_e32 v216, 4, v216
	s_add_u32 s18, s20, s5
	v_lshl_or_b32 v215, v215, 1, v216
	v_add_u32_e32 v216, s26, v212
	s_addc_u32 s19, s21, s19
	v_bfe_u32 v213, v209, 2, 3
	v_lshrrev_b32_e32 v214, 1, v209
	s_xor_b32 s5, s74, 0x4000
	v_lshlrev_b32_e32 v217, 1, v216
	v_lshlrev_b32_e32 v214, 3, v209
	s_add_i32 s5, s5, 0
	v_and_b32_e32 v217, 0xfffff0, v217
	v_and_b32_e32 v216, 4, v216
	v_lshlrev_b32_e32 v216, 1, v216
	v_and_b32_e32 v214, 24, v214
	v_or3_b32 v216, v216, v217, v213
	v_and_b32_e32 v209, 0x60, v209
	s_add_i32 s75, s5, s27
	v_mul_u32_u24_e32 v216, 0x1900, v216
	v_or3_b32 v209, s69, v209, v214
	s_add_i32 m0, s75, 0x8000
	v_add_lshl_u32 v209, v209, v216, 1
	global_load_lds_dwordx4 v215, s[18:19]
	s_mov_b32 m0, s75
	s_add_i32 s5, s5, s30
	global_load_lds_dwordx4 v209, s[18:19]
	v_add_u32_e32 v209, s28, v210
	v_mul_lo_u32 v210, v209, s44
	v_bitop3_b32 v209, v209, v211, 15 bitop3:0x6c
	v_add_u32_e32 v210, s67, v210
	v_lshlrev_b32_e32 v209, 4, v209
	v_lshl_or_b32 v209, v210, 1, v209
	v_add_u32_e32 v210, s29, v212
	v_lshlrev_b32_e32 v211, 1, v210
	v_and_b32_e32 v211, 0xfffff0, v211
	v_and_b32_e32 v212, 4, v210
	v_lshlrev_b32_e32 v212, 1, v212
	v_lshlrev_b32_e32 v210, 5, v210
	v_or3_b32 v211, v212, v211, v213
	v_and_b32_e32 v210, 0x60, v210
	v_mul_u32_u24_e32 v211, 0x1900, v211
	v_or3_b32 v210, s69, v210, v214
	s_add_i32 m0, s5, 0x8000
	v_add_lshl_u32 v210, v210, v211, 1
	global_load_lds_dwordx4 v209, s[18:19]
	s_mov_b32 m0, s5
	s_nop 0
	global_load_lds_dwordx4 v210, s[18:19]

.LBB0_644:
	v_exp_f32_e32 v211, v146
	v_exp_f32_e32 v212, v147
	v_exp_f32_e32 v213, v148
	v_exp_f32_e32 v214, v149
	v_exp_f32_e32 v215, v150
	v_exp_f32_e32 v216, v151
	v_exp_f32_e32 v217, v152
	v_exp_f32_e32 v218, v153
	v_exp_f32_e32 v219, v154
	v_exp_f32_e32 v220, v155
	v_exp_f32_e32 v221, v156
	v_exp_f32_e32 v222, v157
	v_exp_f32_e32 v223, v158
	v_exp_f32_e32 v224, v159
	v_exp_f32_e32 v225, v160
	v_exp_f32_e32 v226, v161
	v_exp_f32_e32 v227, v130
	v_exp_f32_e32 v228, v131
	v_exp_f32_e32 v229, v132
	v_exp_f32_e32 v230, v133
	v_exp_f32_e32 v231, v134
	v_exp_f32_e32 v232, v135
	v_exp_f32_e32 v233, v136
	v_exp_f32_e32 v234, v137
	v_exp_f32_e32 v235, v138
	v_exp_f32_e32 v236, v139
	v_exp_f32_e32 v237, v140
	v_exp_f32_e32 v238, v141
	v_exp_f32_e32 v239, v142
	v_exp_f32_e32 v240, v143
	v_exp_f32_e32 v241, v144
	v_exp_f32_e32 v210, v145
	v_cvt_pk_bf16_f32 v130, v211, v212
	v_cvt_pk_bf16_f32 v131, v213, v214
	v_cvt_pk_bf16_f32 v132, v215, v216
	v_cvt_pk_bf16_f32 v133, v217, v218
	v_cvt_pk_bf16_f32 v134, v219, v220
	v_cvt_pk_bf16_f32 v135, v221, v222
	v_cvt_pk_bf16_f32 v136, v223, v224
	v_cvt_pk_bf16_f32 v137, v225, v226
	v_cvt_pk_bf16_f32 v138, v227, v228
	v_cvt_pk_bf16_f32 v139, v229, v230
	v_cvt_pk_bf16_f32 v140, v231, v232
	v_cvt_pk_bf16_f32 v141, v233, v234
	v_cvt_pk_bf16_f32 v142, v235, v236
	v_cvt_pk_bf16_f32 v143, v237, v238
	v_cvt_pk_bf16_f32 v144, v239, v240
	v_cvt_pk_bf16_f32 v145, v241, v210
	s_nop 0
	s_setprio 1
	v_add_u32_e32 v209, s74, v195
	ds_read_b64_tr_b16 v[146:147], v209 offset:0
	ds_read_b64_tr_b16 v[148:149], v209 offset:0x800
	ds_read_b64_tr_b16 v[150:151], v209 offset:0x1000
	ds_read_b64_tr_b16 v[152:153], v209 offset:0x1800
	ds_read_b64_tr_b16 v[154:155], v209 offset:0x2000
	ds_read_b64_tr_b16 v[156:157], v209 offset:0x2800
	ds_read_b64_tr_b16 v[158:159], v209 offset:0x3000
	ds_read_b64_tr_b16 v[160:161], v209 offset:0x3800
	s_waitcnt lgkmcnt(0)
	s_nop 0
	v_mfma_f32_32x32x16_bf16 v[82:97], v[130:133], v[146:149], v[82:97]
	ds_read_b64_tr_b16 v[146:147], v209 offset:0x200
	ds_read_b64_tr_b16 v[148:149], v209 offset:0xa00
	v_mfma_f32_32x32x16_bf16 v[82:97], v[134:137], v[150:153], v[82:97]
	ds_read_b64_tr_b16 v[150:151], v209 offset:0x1200
	ds_read_b64_tr_b16 v[152:153], v209 offset:0x1a00
	v_mfma_f32_32x32x16_bf16 v[82:97], v[138:141], v[154:157], v[82:97]
	ds_read_b64_tr_b16 v[154:155], v209 offset:0x2200
	ds_read_b64_tr_b16 v[156:157], v209 offset:0x2a00
	ds_read_b64_tr_b16 v[242:243], v209 offset:0x3200
	ds_read_b64_tr_b16 v[244:245], v209 offset:0x3a00
	s_waitcnt lgkmcnt(0)
	v_mfma_f32_32x32x16_bf16 v[82:97], v[142:145], v[158:161], v[82:97]
	v_mfma_f32_32x32x16_bf16 v[66:81], v[130:133], v[146:149], v[66:81]
	ds_read_b64_tr_b16 v[146:147], v209 offset:0x400
	ds_read_b64_tr_b16 v[148:149], v209 offset:0xc00
	v_mfma_f32_32x32x16_bf16 v[66:81], v[134:137], v[150:153], v[66:81]
	ds_read_b64_tr_b16 v[150:151], v209 offset:0x1400
	ds_read_b64_tr_b16 v[152:153], v209 offset:0x1c00
	v_mfma_f32_32x32x16_bf16 v[66:81], v[138:141], v[154:157], v[66:81]
	ds_read_b64_tr_b16 v[154:155], v209 offset:0x2400
	ds_read_b64_tr_b16 v[156:157], v209 offset:0x2c00
	ds_read_b64_tr_b16 v[158:159], v209 offset:0x3400
	ds_read_b64_tr_b16 v[160:161], v209 offset:0x3c00
	s_waitcnt lgkmcnt(0)
	v_mfma_f32_32x32x16_bf16 v[66:81], v[142:145], v[242:245], v[66:81]
	v_mfma_f32_32x32x16_bf16 v[98:113], v[130:133], v[146:149], v[98:113]
	ds_read_b64_tr_b16 v[146:147], v209 offset:0x600
	ds_read_b64_tr_b16 v[148:149], v209 offset:0xe00
	v_mfma_f32_32x32x16_bf16 v[98:113], v[134:137], v[150:153], v[98:113]
	ds_read_b64_tr_b16 v[150:151], v209 offset:0x1600
	ds_read_b64_tr_b16 v[152:153], v209 offset:0x1e00
	v_mfma_f32_32x32x16_bf16 v[98:113], v[138:141], v[154:157], v[98:113]
	ds_read_b64_tr_b16 v[154:155], v209 offset:0x2600
	ds_read_b64_tr_b16 v[156:157], v209 offset:0x2e00
	ds_read_b64_tr_b16 v[242:243], v209 offset:0x3600
	ds_read_b64_tr_b16 v[244:245], v209 offset:0x3e00
	s_waitcnt lgkmcnt(0)
	v_mfma_f32_32x32x16_bf16 v[98:113], v[142:145], v[158:161], v[98:113]
	v_mfma_f32_32x32x16_bf16 v[114:129], v[130:133], v[146:149], v[114:129]
	v_add_u32_e32 v130, s73, v188
	ds_read_b128 v[130:133], v130 offset:32768
	v_add_u32_e32 v246, s24, v190
	ds_read_b128 v[246:249], v246
	v_add3_u32 v250, s73, v189, v178
	v_mfma_f32_32x32x16_bf16 v[114:129], v[134:137], v[150:153], v[114:129]
	v_add_u32_e32 v134, s24, v188
	ds_read_b128 v[134:137], v134
	v_mfma_f32_32x32x16_bf16 v[114:129], v[138:141], v[154:157], v[114:129]
	v_add3_u32 v138, s73, v187, v178
	v_mfma_f32_32x32x16_bf16 v[114:129], v[142:145], v[242:245], v[114:129]
	v_add_u32_e32 v242, s73, v190
	ds_read_b128 v[242:245], v242 offset:32768
	s_waitcnt lgkmcnt(0)
	v_mfma_f32_32x32x16_bf16 v[146:161], v[130:133], v[134:137], 0
	ds_read_b128 v[130:133], v138 offset:40960
	v_mfma_f32_32x32x16_bf16 v[146:161], v[242:245], v[246:249], v[146:161]
	ds_read_b128 v[242:245], v250 offset:40960
	v_add3_u32 v250, s73, v191, v178
	s_waitcnt lgkmcnt(0)
	v_mfma_f32_32x32x16_bf16 v[130:145], v[130:133], v[134:137], 0
	v_mfma_f32_32x32x16_bf16 v[130:145], v[242:245], v[246:249], v[130:145]
	v_add_u32_e32 v242, s73, v192
	ds_read_b128 v[242:245], v242 offset:32768
	v_add_u32_e32 v246, s24, v192
	ds_read_b128 v[246:249], v246
	s_waitcnt lgkmcnt(0)
	v_mfma_f32_32x32x16_bf16 v[146:161], v[242:245], v[246:249], v[146:161]
	ds_read_b128 v[242:245], v250 offset:40960
	v_add3_u32 v250, s73, v193, v178
	s_waitcnt lgkmcnt(0)
	v_mfma_f32_32x32x16_bf16 v[130:145], v[242:245], v[246:249], v[130:145]
	v_add_u32_e32 v242, s73, v194
	ds_read_b128 v[242:245], v242 offset:32768
	v_add_u32_e32 v246, s24, v194
	ds_read_b128 v[246:249], v246
	s_waitcnt lgkmcnt(0)
	v_mfma_f32_32x32x16_bf16 v[146:161], v[242:245], v[246:249], v[146:161]
	ds_read_b128 v[242:245], v250 offset:40960
	s_waitcnt lgkmcnt(0)
	v_mfma_f32_32x32x16_bf16 v[130:145], v[242:245], v[246:249], v[130:145]
	s_setprio 0
	s_and_b64 vcc, exec, s[4:5]
	s_cbranch_vccz .LBB0_649
	s_and_b64 vcc, exec, s[4:5]
	s_cbranch_vccz .LBB0_650
.LBB0_646:
	v_add_f32_e32 v211, 0, v211
	v_add_f32_e32 v211, v212, v211
	v_add_f32_e32 v211, v213, v211
	v_add_f32_e32 v211, v214, v211
	v_add_f32_e32 v211, v215, v211
	v_add_f32_e32 v211, v216, v211
	v_add_f32_e32 v211, v217, v211
	v_add_f32_e32 v211, v218, v211
	v_add_f32_e32 v211, v219, v211
	v_add_f32_e32 v211, v220, v211
	v_add_f32_e32 v211, v221, v211
	v_add_f32_e32 v211, v222, v211
	v_add_f32_e32 v211, v223, v211
	v_add_f32_e32 v211, v224, v211
	v_add_f32_e32 v211, v225, v211
	v_add_f32_e32 v211, v226, v211
	v_add_f32_e32 v211, v211, v227
	v_add_f32_e32 v211, v228, v211
	v_add_f32_e32 v211, v229, v211
	v_add_f32_e32 v211, v230, v211
	v_add_f32_e32 v211, v231, v211
	v_add_f32_e32 v211, v232, v211
	v_add_f32_e32 v211, v233, v211
	v_add_f32_e32 v211, v234, v211
	v_add_f32_e32 v211, v235, v211
	v_add_f32_e32 v211, v236, v211
	v_add_f32_e32 v211, v237, v211
	v_add_f32_e32 v211, v238, v211
	v_add_f32_e32 v211, v239, v211
	v_add_f32_e32 v211, v240, v211
	v_add_f32_e32 v211, v241, v211
	v_exp_f32_e32 v212, v130
	v_add_f32_e32 v130, v210, v211
	v_add_f32_e32 v207, v207, v130
	s_add_i32 s72, s72, 1
	v_exp_f32_e32 v146, v146
	v_exp_f32_e32 v147, v147
	v_exp_f32_e32 v148, v148
	v_exp_f32_e32 v149, v149
	v_exp_f32_e32 v150, v150
	v_exp_f32_e32 v151, v151
	v_exp_f32_e32 v152, v152
	v_exp_f32_e32 v153, v153
	v_exp_f32_e32 v154, v154
	v_exp_f32_e32 v155, v155
	v_exp_f32_e32 v156, v156
	v_exp_f32_e32 v157, v157
	v_exp_f32_e32 v158, v158
	v_exp_f32_e32 v159, v159
	v_exp_f32_e32 v160, v160
	v_exp_f32_e32 v161, v161
	v_exp_f32_e32 v213, v131
	v_exp_f32_e32 v214, v132
	v_exp_f32_e32 v215, v133
	v_exp_f32_e32 v216, v134
	v_exp_f32_e32 v217, v135
	v_exp_f32_e32 v218, v136
	v_exp_f32_e32 v219, v137
	v_exp_f32_e32 v220, v138
	v_exp_f32_e32 v221, v139
	v_exp_f32_e32 v222, v140
	v_exp_f32_e32 v223, v141
	v_exp_f32_e32 v224, v142
	v_exp_f32_e32 v225, v143
	v_exp_f32_e32 v226, v144
	v_exp_f32_e32 v145, v145
	v_add_f32_e32 v130, 0, v146
	v_add_f32_e32 v130, v147, v130
	v_add_f32_e32 v130, v148, v130
	v_add_f32_e32 v130, v149, v130
	v_add_f32_e32 v130, v150, v130
	v_add_f32_e32 v130, v151, v130
	v_add_f32_e32 v130, v152, v130
	v_add_f32_e32 v130, v153, v130
	v_add_f32_e32 v130, v154, v130
	v_add_f32_e32 v130, v155, v130
	v_add_f32_e32 v130, v156, v130
	v_add_f32_e32 v130, v157, v130
	v_add_f32_e32 v130, v158, v130
	v_add_f32_e32 v130, v159, v130
	v_add_f32_e32 v130, v160, v130
	v_add_f32_e32 v130, v161, v130
	v_add_f32_e32 v130, v130, v212
	v_add_f32_e32 v130, v213, v130
	v_add_f32_e32 v130, v214, v130
	v_add_f32_e32 v130, v215, v130
	v_add_f32_e32 v130, v216, v130
	v_add_f32_e32 v130, v217, v130
	v_add_f32_e32 v130, v218, v130
	v_add_f32_e32 v130, v219, v130
	v_add_f32_e32 v130, v220, v130
	v_add_f32_e32 v130, v221, v130
	v_add_f32_e32 v130, v222, v130
	v_add_f32_e32 v130, v223, v130
	v_add_f32_e32 v130, v224, v130
	v_add_f32_e32 v130, v225, v130
	v_add_f32_e32 v130, v226, v130
	v_add_f32_e32 v130, v145, v130
	v_add_f32_e32 v206, v206, v130
	v_cvt_pk_bf16_f32 v130, v146, v147
	v_cvt_pk_bf16_f32 v131, v148, v149
	v_cvt_pk_bf16_f32 v132, v150, v151
	v_cvt_pk_bf16_f32 v133, v152, v153
	v_cvt_pk_bf16_f32 v134, v154, v155
	v_cvt_pk_bf16_f32 v135, v156, v157
	v_cvt_pk_bf16_f32 v136, v158, v159
	v_cvt_pk_bf16_f32 v137, v160, v161
	v_cvt_pk_bf16_f32 v138, v212, v213
	v_cvt_pk_bf16_f32 v139, v214, v215
	v_cvt_pk_bf16_f32 v140, v216, v217
	v_cvt_pk_bf16_f32 v141, v218, v219
	v_cvt_pk_bf16_f32 v142, v220, v221
	v_cvt_pk_bf16_f32 v143, v222, v223
	v_cvt_pk_bf16_f32 v144, v224, v225
	v_cvt_pk_bf16_f32 v145, v226, v145
	s_nop 0
	s_setprio 1
	ds_read_b64_tr_b16 v[146:147], v209 offset:0
	ds_read_b64_tr_b16 v[148:149], v209 offset:0x800
	ds_read_b64_tr_b16 v[150:151], v209 offset:0x1000
	ds_read_b64_tr_b16 v[152:153], v209 offset:0x1800
	ds_read_b64_tr_b16 v[154:155], v209 offset:0x2000
	ds_read_b64_tr_b16 v[156:157], v209 offset:0x2800
	ds_read_b64_tr_b16 v[158:159], v209 offset:0x3000
	ds_read_b64_tr_b16 v[160:161], v209 offset:0x3800
	s_waitcnt lgkmcnt(0)
	s_nop 0
	v_mfma_f32_32x32x16_bf16 v[50:65], v[130:133], v[146:149], v[50:65]
	ds_read_b64_tr_b16 v[146:147], v209 offset:0x200
	ds_read_b64_tr_b16 v[148:149], v209 offset:0xa00
	v_mfma_f32_32x32x16_bf16 v[50:65], v[134:137], v[150:153], v[50:65]
	ds_read_b64_tr_b16 v[150:151], v209 offset:0x1200
	ds_read_b64_tr_b16 v[152:153], v209 offset:0x1a00
	v_mfma_f32_32x32x16_bf16 v[50:65], v[138:141], v[154:157], v[50:65]
	ds_read_b64_tr_b16 v[154:155], v209 offset:0x2200
	ds_read_b64_tr_b16 v[156:157], v209 offset:0x2a00
	ds_read_b64_tr_b16 v[210:211], v209 offset:0x3200
	ds_read_b64_tr_b16 v[212:213], v209 offset:0x3a00
	s_waitcnt lgkmcnt(0)
	v_mfma_f32_32x32x16_bf16 v[50:65], v[142:145], v[158:161], v[50:65]
	v_mfma_f32_32x32x16_bf16 v[34:49], v[130:133], v[146:149], v[34:49]
	ds_read_b64_tr_b16 v[146:147], v209 offset:0x400
	ds_read_b64_tr_b16 v[148:149], v209 offset:0xc00
	v_mfma_f32_32x32x16_bf16 v[34:49], v[134:137], v[150:153], v[34:49]
	ds_read_b64_tr_b16 v[150:151], v209 offset:0x1400
	ds_read_b64_tr_b16 v[152:153], v209 offset:0x1c00
	v_mfma_f32_32x32x16_bf16 v[34:49], v[138:141], v[154:157], v[34:49]
	ds_read_b64_tr_b16 v[154:155], v209 offset:0x2400
	ds_read_b64_tr_b16 v[156:157], v209 offset:0x2c00
	ds_read_b64_tr_b16 v[158:159], v209 offset:0x3400
	ds_read_b64_tr_b16 v[160:161], v209 offset:0x3c00
	s_waitcnt lgkmcnt(0)
	v_mfma_f32_32x32x16_bf16 v[34:49], v[142:145], v[210:213], v[34:49]
	v_mfma_f32_32x32x16_bf16 v[18:33], v[130:133], v[146:149], v[18:33]
	ds_read_b64_tr_b16 v[146:147], v209 offset:0x600
	ds_read_b64_tr_b16 v[148:149], v209 offset:0xe00
	v_mfma_f32_32x32x16_bf16 v[18:33], v[134:137], v[150:153], v[18:33]
	ds_read_b64_tr_b16 v[150:151], v209 offset:0x1600
	ds_read_b64_tr_b16 v[152:153], v209 offset:0x1e00
	v_mfma_f32_32x32x16_bf16 v[18:33], v[138:141], v[154:157], v[18:33]
	ds_read_b64_tr_b16 v[154:155], v209 offset:0x2600
	ds_read_b64_tr_b16 v[156:157], v209 offset:0x2e00
	ds_read_b64_tr_b16 v[210:211], v209 offset:0x3600
	ds_read_b64_tr_b16 v[212:213], v209 offset:0x3e00
	s_waitcnt lgkmcnt(0)
	v_mfma_f32_32x32x16_bf16 v[18:33], v[142:145], v[158:161], v[18:33]
	v_mfma_f32_32x32x16_bf16 v[2:17], v[130:133], v[146:149], v[2:17]
	v_mfma_f32_32x32x16_bf16 v[2:17], v[134:137], v[150:153], v[2:17]
	v_mfma_f32_32x32x16_bf16 v[2:17], v[138:141], v[154:157], v[2:17]
	v_mfma_f32_32x32x16_bf16 v[2:17], v[142:145], v[210:213], v[2:17]
	s_setprio 0
	s_waitcnt vmcnt(0)
	s_add_i32 s71, s71, 64
	s_addk_i32 s70, 0x4000
	s_cmpk_eq_i32 s72, 0x44
	s_waitcnt vmcnt(0)
	s_barrier
	s_cbranch_scc0 .LBB0_640
	s_branch .LBB0_651
